# plucker K-loop register double-buffered (reads of tile k+1 and DMA refill interleaved with MFMAs of tile k)
# speedup vs baseline: 1.0362x; 1.0071x over previous
_Z12gemm1_kernel6G1Args:
	s_load_dwordx2 s[24:25], s[0:1], 0x8
	s_load_dwordx16 s[8:23], s[0:1], 0x18
	s_ashr_i32 s3, s2, 3
	v_and_b32_e32 v42, 15, v0
	v_bfe_u32 v1, v0, 4, 2
	v_lshrrev_b32_e32 v78, 8, v0
	s_mov_b64 s[4:5], -1
	s_cmp_gt_i32 s3, 23
	v_lshrrev_b32_e32 v44, 4, v0
	v_lshrrev_b32_e32 v43, 1, v0
	v_lshlrev_b32_e32 v79, 4, v0
	s_cbranch_scc0 .LBB1_32
	s_lshl_b32 s4, s2, 8
	s_and_b32 s4, s4, 0x700
	s_lshl_b32 s5, s3, 5
	s_add_i32 s33, s5, s4
	s_addk_i32 s33, 0xfd00
	s_load_dwordx2 s[26:27], s[0:1], 0x10
	s_bfe_u32 s28, s2, 0x10003
	s_and_b32 s39, s33, 0xffffffc0
	s_and_b32 s7, 8, s2
	s_cmp_eq_u32 s28, 0
	s_cselect_b64 s[4:5], -1, 0
	s_cmp_lg_u32 s7, 0
	s_cselect_b64 s[6:7], -1, 0
	s_mul_i32 s28, s28, 0xc0000
	v_lshrrev_b32_e32 v45, 6, v0
	v_sub_u32_e32 v2, 0, v44
	v_xor_b32_e32 v2, v0, v2
	v_lshlrev_b32_e32 v2, 3, v2
	v_and_b32_e32 v8, 24, v2
	v_lshrrev_b32_e32 v14, 2, v0
	v_mul_u32_u24_e32 v3, 0xc00, v14
	v_or_b32_e32 v2, v3, v8
	v_lshlrev_b32_e32 v2, 1, v2
	v_mov_b32_e32 v3, 0
	v_readfirstlane_b32 s41, v79
	v_readfirstlane_b32 s30, v45
	s_waitcnt lgkmcnt(0)
	s_add_u32 s26, s26, s28
	s_addc_u32 s27, s27, 0
	v_lshl_add_u64 v[4:5], s[26:27], 0, v[2:3]
	v_add_u32_e32 v2, 0x1000, v2
	v_lshl_add_u64 v[6:7], s[26:27], 0, v[2:3]
	v_bfe_u32 v9, v0, 2, 6
	v_add_u32_e32 v9, s39, v9
	v_lshlrev_b32_e32 v9, 12, v9
	v_lshl_or_b32 v9, v78, 11, v9
	v_lshl_or_b32 v2, v8, 1, v9
	v_lshl_add_u64 v[8:9], s[24:25], 0, v[2:3]
	s_add_i32 s28, s39, -1
	s_max_i32 s28, s28, 0
	s_lshl_b32 s28, s28, 12
	v_and_b32_e32 v2, 0xff, v0
	v_lshlrev_b32_e32 v2, 4, v2
	v_add_u32_e32 v2, s28, v2
	v_lshl_add_u64 v[10:11], s[24:25], 0, v[2:3]
	s_bfe_u32 s31, s30, 0x10001
	s_lshl_b32 s31, s31, 12
	s_and_b32 s34, s30, 1
	s_lshl_b32 s34, s34, 10
	s_or_b32 s31, s31, s34
	s_bfe_u32 s34, s30, 0x10002
	s_lshl_b32 s34, s34, 11
	s_or_b32 s31, s31, s34
	s_add_u32 s40, s31, 0x4000
	s_and_b32 s34, s41, 0xc00
	s_add_u32 s34, s34, 0x6000
	s_mov_b32 m0, s34
	s_add_u32 s35, s41, 0x2000
	global_load_lds_dwordx4 v[10:11], off
	s_mov_b32 m0, s41
	s_mov_b64 s[26:27], 0x80
	global_load_lds_dwordx4 v[4:5], off
	s_mov_b32 m0, s35
	s_mov_b64 s[28:29], 0xc0
	global_load_lds_dwordx4 v[6:7], off
	s_mov_b32 m0, s40
	s_mov_b64 s[30:31], 0x100
	global_load_lds_dwordx4 v[8:9], off
	s_add_u32 m0, s41, 0x8000
	v_lshl_add_u64 v[12:13], v[4:5], 0, 64
	global_load_lds_dwordx4 v[12:13], off
	s_add_u32 m0, s35, 0x8000
	v_lshl_add_u64 v[12:13], v[6:7], 0, 64
	global_load_lds_dwordx4 v[12:13], off
	s_add_u32 m0, s40, 0x8000
	v_lshl_add_u64 v[12:13], v[8:9], 0, 64
	global_load_lds_dwordx4 v[12:13], off
	s_add_u32 m0, s41, 0x10000
	v_lshl_add_u64 v[12:13], v[4:5], 0, s[26:27]
	global_load_lds_dwordx4 v[12:13], off
	s_add_u32 m0, s35, 0x10000
	v_lshl_add_u64 v[12:13], v[6:7], 0, s[26:27]
	global_load_lds_dwordx4 v[12:13], off
	s_add_u32 m0, s40, 0x10000
	v_lshl_add_u64 v[12:13], v[8:9], 0, s[26:27]
	global_load_lds_dwordx4 v[12:13], off
	s_add_u32 m0, s41, 0x18000
	v_lshl_add_u64 v[12:13], v[4:5], 0, s[28:29]
	global_load_lds_dwordx4 v[12:13], off
	s_add_u32 m0, s35, 0x18000
	v_lshl_add_u64 v[12:13], v[6:7], 0, s[28:29]
	global_load_lds_dwordx4 v[12:13], off
	s_add_u32 m0, s40, 0x18000
	v_lshl_add_u64 v[12:13], v[8:9], 0, s[28:29]
	global_load_lds_dwordx4 v[12:13], off
	s_add_u32 m0, s41, 0x20000
	v_lshl_add_u64 v[12:13], v[4:5], 0, s[30:31]
	global_load_lds_dwordx4 v[12:13], off
	s_add_u32 m0, s35, 0x20000
	v_lshl_add_u64 v[12:13], v[6:7], 0, s[30:31]
	global_load_lds_dwordx4 v[12:13], off
	s_add_u32 m0, s40, 0x20000
	v_lshl_add_u64 v[12:13], v[8:9], 0, s[30:31]
	global_load_lds_dwordx4 v[12:13], off
	s_mov_b64 s[26:27], 0x140
	v_lshl_add_u64 v[36:37], v[8:9], 0, s[26:27]
	v_lshl_add_u64 v[38:39], v[6:7], 0, s[26:27]
	v_lshl_add_u64 v[40:41], v[4:5], 0, s[26:27]
	s_mov_b64 s[26:27], 0
	v_lshlrev_b32_e32 v48, 6, v78
	v_and_b32_e32 v47, 32, v14
	v_and_b32_e32 v49, 32, v43
	v_and_b32_e32 v46, 63, v0
	v_or_b32_e32 v2, v48, v42
	v_or_b32_e32 v12, v2, v47
	v_lshlrev_b32_e32 v50, 6, v12
	v_sub_u32_e32 v13, 0, v14
	v_bitop3_b32 v13, v13, v1, 3 bitop3:0x6c
	v_lshlrev_b32_e32 v52, 4, v13
	v_cmp_eq_u32_e32 vcc, 0, v78
	s_and_b64 s[34:35], vcc, s[4:5]
	v_cndmask_b32_e64 v88, 0, 1, s[34:35]
	v_add_u32_e32 v89, v49, v42
	v_sub_u32_e32 v89, v89, v88
	v_cmp_eq_u32_e64 s[42:43], -1, v89
	v_and_b32_e32 v90, 32, v89
	v_lshlrev_b32_e32 v90, 7, v90
	v_and_b32_e32 v91, 31, v89
	v_lshl_or_b32 v90, v91, 6, v90
	v_ashrrev_i32_e32 v91, 2, v89
	v_sub_u32_e32 v91, 0, v91
	v_xor_b32_e32 v91, v91, v1
	v_and_b32_e32 v91, 3, v91
	v_lshl_or_b32 v92, v91, 4, v90
	v_add_u32_e32 v89, 16, v89
	v_and_b32_e32 v90, 32, v89
	v_lshlrev_b32_e32 v90, 7, v90
	v_and_b32_e32 v94, 31, v89
	v_lshl_or_b32 v90, v94, 6, v90
	v_lshl_or_b32 v93, v91, 4, v90
	v_lshlrev_b32_e32 v95, 4, v1
	v_add_u32_e32 v95, 0x2000, v95
	s_mov_b32 s36, 0
	s_mov_b32 s37, 0
	s_mov_b32 s38, 1
	s_mov_b32 s28, 0
	v_mov_b32_e32 v2, v3
	v_mov_b32_e32 v4, v3
	v_mov_b32_e32 v5, v3
	v_mov_b32_e32 v6, v3
	v_mov_b32_e32 v7, v3
	v_mov_b32_e32 v8, v3
	v_mov_b32_e32 v9, v3
	v_mov_b32_e32 v10, v3
	v_mov_b32_e32 v11, v3
	v_mov_b32_e32 v12, v3
	v_mov_b32_e32 v13, v3
	v_mov_b32_e32 v14, v3
	v_mov_b32_e32 v15, v3
	v_mov_b32_e32 v16, v3
	v_mov_b32_e32 v17, v3
	v_mov_b32_e32 v18, v3
	v_mov_b32_e32 v19, v3
	v_mov_b32_e32 v20, v3
	v_mov_b32_e32 v21, v3
	v_mov_b32_e32 v22, v3
	v_mov_b32_e32 v23, v3
	v_mov_b32_e32 v24, v3
	v_mov_b32_e32 v25, v3
	v_mov_b32_e32 v26, v3
	v_mov_b32_e32 v27, v3
	v_mov_b32_e32 v28, v3
	v_mov_b32_e32 v29, v3
	v_mov_b32_e32 v30, v3
	v_mov_b32_e32 v31, v3
	v_mov_b32_e32 v32, v3
	v_mov_b32_e32 v33, v3
	s_waitcnt vmcnt(12)
	s_barrier
	v_or_b32_e32 v53, s28, v50
	v_add_u32_e32 v88, s28, v92
	v_add_u32_e32 v53, v53, v52
	v_add_u32_e32 v89, s28, v93
	v_cndmask_b32_e64 v88, v88, v95, s[42:43]
	v_add_u32_e32 v95, 64, v95
	ds_read_b128 v[54:57], v53
	ds_read_b128 v[58:61], v88 offset:16384
	ds_read_b128 v[62:65], v53 offset:1024
	ds_read_b128 v[66:69], v89 offset:16384
	ds_read_b128 v[70:73], v88 offset:18432
	ds_read_b128 v[74:77], v89 offset:18432
	ds_read_b128 v[80:83], v53 offset:8192
	ds_read_b128 v[84:87], v53 offset:9216
.LBB1_2:
	s_waitcnt vmcnt(9)
	s_waitcnt lgkmcnt(0)
	s_barrier
	s_lshl_b32 s28, s38, 15
	v_or_b32_e32 v53, s28, v50
	v_add_u32_e32 v88, s28, v92
	v_add_u32_e32 v53, v53, v52
	v_add_u32_e32 v89, s28, v93
	v_cndmask_b32_e64 v88, v88, v95, s[42:43]
	v_add_u32_e32 v95, 64, v95
	s_lshl_b32 s29, s37, 15
	s_add_u32 s30, s29, s41
	s_add_u32 s31, s29, s40
	ds_read_b128 v[100:103], v53
	ds_read_b128 v[104:107], v88 offset:16384
	v_mfma_f32_16x16x32_f16 v[14:17], v[62:65], v[58:61], v[14:17]
	ds_read_b128 v[108:111], v53 offset:1024
	v_mfma_f32_16x16x32_f16 v[30:33], v[54:57], v[58:61], v[30:33]
	ds_read_b128 v[112:115], v89 offset:16384
	v_mfma_f32_16x16x32_f16 v[22:25], v[54:57], v[66:69], v[22:25]
	ds_read_b128 v[116:119], v88 offset:18432
	v_mfma_f32_16x16x32_f16 v[6:9], v[62:65], v[66:69], v[6:9]
	ds_read_b128 v[120:123], v89 offset:18432
	v_mfma_f32_16x16x32_f16 v[26:29], v[54:57], v[70:73], v[26:29]
	ds_read_b128 v[124:127], v53 offset:8192
	v_mfma_f32_16x16x32_f16 v[30:33], v[80:83], v[58:61], v[30:33]
	ds_read_b128 v[128:131], v53 offset:9216
	v_mfma_f32_16x16x32_f16 v[22:25], v[80:83], v[66:69], v[22:25]
	s_mov_b32 m0, s30
	v_lshl_add_u64 v[96:97], v[40:41], 0, s[26:27]
	global_load_lds_dwordx4 v[96:97], off
	v_mfma_f32_16x16x32_f16 v[18:21], v[54:57], v[74:77], v[18:21]
	s_add_u32 m0, s30, 0x2000
	v_lshl_add_u64 v[96:97], v[38:39], 0, s[26:27]
	global_load_lds_dwordx4 v[96:97], off
	v_mfma_f32_16x16x32_f16 v[14:17], v[84:87], v[58:61], v[14:17]
	s_mov_b32 m0, s31
	v_lshl_add_u64 v[96:97], v[36:37], 0, s[26:27]
	global_load_lds_dwordx4 v[96:97], off
	v_mfma_f32_16x16x32_f16 v[10:13], v[62:65], v[70:73], v[10:13]
	v_mfma_f32_16x16x32_f16 v[6:9], v[84:87], v[66:69], v[6:9]
	v_mfma_f32_16x16x32_f16 v[2:5], v[62:65], v[74:77], v[2:5]
	s_add_i32 s36, s36, 1
	s_add_u32 s26, s26, 64
	s_add_i32 s28, s37, 1
	s_cmp_lg_u32 s37, 4
	s_cselect_b32 s37, s28, 0
	s_add_i32 s28, s38, 1
	s_cmp_lg_u32 s38, 4
	s_cselect_b32 s38, s28, 0
	s_waitcnt vmcnt(9)
	s_waitcnt lgkmcnt(0)
	s_barrier
	s_lshl_b32 s28, s38, 15
	v_or_b32_e32 v53, s28, v50
	v_add_u32_e32 v88, s28, v92
	v_add_u32_e32 v53, v53, v52
	v_add_u32_e32 v89, s28, v93
	v_cndmask_b32_e64 v88, v88, v95, s[42:43]
	v_add_u32_e32 v95, 64, v95
	s_lshl_b32 s29, s37, 15
	s_add_u32 s30, s29, s41
	s_add_u32 s31, s29, s40
	ds_read_b128 v[54:57], v53
	ds_read_b128 v[58:61], v88 offset:16384
	v_mfma_f32_16x16x32_f16 v[14:17], v[108:111], v[104:107], v[14:17]
	ds_read_b128 v[62:65], v53 offset:1024
	v_mfma_f32_16x16x32_f16 v[30:33], v[100:103], v[104:107], v[30:33]
	ds_read_b128 v[66:69], v89 offset:16384
	v_mfma_f32_16x16x32_f16 v[22:25], v[100:103], v[112:115], v[22:25]
	ds_read_b128 v[70:73], v88 offset:18432
	v_mfma_f32_16x16x32_f16 v[6:9], v[108:111], v[112:115], v[6:9]
	ds_read_b128 v[74:77], v89 offset:18432
	v_mfma_f32_16x16x32_f16 v[26:29], v[100:103], v[116:119], v[26:29]
	ds_read_b128 v[80:83], v53 offset:8192
	v_mfma_f32_16x16x32_f16 v[30:33], v[124:127], v[104:107], v[30:33]
	ds_read_b128 v[84:87], v53 offset:9216
	v_mfma_f32_16x16x32_f16 v[22:25], v[124:127], v[112:115], v[22:25]
	s_mov_b32 m0, s30
	v_lshl_add_u64 v[96:97], v[40:41], 0, s[26:27]
	global_load_lds_dwordx4 v[96:97], off
	v_mfma_f32_16x16x32_f16 v[18:21], v[100:103], v[120:123], v[18:21]
	s_add_u32 m0, s30, 0x2000
	v_lshl_add_u64 v[96:97], v[38:39], 0, s[26:27]
	global_load_lds_dwordx4 v[96:97], off
	v_mfma_f32_16x16x32_f16 v[14:17], v[128:131], v[104:107], v[14:17]
	s_mov_b32 m0, s31
	v_lshl_add_u64 v[96:97], v[36:37], 0, s[26:27]
	global_load_lds_dwordx4 v[96:97], off
	v_mfma_f32_16x16x32_f16 v[10:13], v[108:111], v[116:119], v[10:13]
	v_mfma_f32_16x16x32_f16 v[6:9], v[128:131], v[112:115], v[6:9]
	v_mfma_f32_16x16x32_f16 v[2:5], v[108:111], v[120:123], v[2:5]
	s_add_i32 s36, s36, 1
	s_add_u32 s26, s26, 64
	s_add_i32 s28, s37, 1
	s_cmp_lg_u32 s37, 4
	s_cselect_b32 s37, s28, 0
	s_add_i32 s28, s38, 1
	s_cmp_lg_u32 s38, 4
	s_cselect_b32 s38, s28, 0
	s_cmp_lt_u32 s36, 26
	s_cbranch_scc1 .LBB1_2
	s_waitcnt vmcnt(9)
	s_waitcnt lgkmcnt(0)
	s_barrier
	s_lshl_b32 s28, s38, 15
	v_or_b32_e32 v53, s28, v50
	v_add_u32_e32 v88, s28, v92
	v_add_u32_e32 v53, v53, v52
	v_add_u32_e32 v89, s28, v93
	v_cndmask_b32_e64 v88, v88, v95, s[42:43]
	v_add_u32_e32 v95, 64, v95
	s_lshl_b32 s29, s37, 15
	s_add_u32 s30, s29, s41
	s_add_u32 s31, s29, s40
	ds_read_b128 v[100:103], v53
	ds_read_b128 v[104:107], v88 offset:16384
	v_mfma_f32_16x16x32_f16 v[14:17], v[62:65], v[58:61], v[14:17]
	ds_read_b128 v[108:111], v53 offset:1024
	v_mfma_f32_16x16x32_f16 v[30:33], v[54:57], v[58:61], v[30:33]
	ds_read_b128 v[112:115], v89 offset:16384
	v_mfma_f32_16x16x32_f16 v[22:25], v[54:57], v[66:69], v[22:25]
	ds_read_b128 v[116:119], v88 offset:18432
	v_mfma_f32_16x16x32_f16 v[6:9], v[62:65], v[66:69], v[6:9]
	ds_read_b128 v[120:123], v89 offset:18432
	v_mfma_f32_16x16x32_f16 v[26:29], v[54:57], v[70:73], v[26:29]
	ds_read_b128 v[124:127], v53 offset:8192
	v_mfma_f32_16x16x32_f16 v[30:33], v[80:83], v[58:61], v[30:33]
	ds_read_b128 v[128:131], v53 offset:9216
	v_mfma_f32_16x16x32_f16 v[22:25], v[80:83], v[66:69], v[22:25]
	s_mov_b32 m0, s30
	v_lshl_add_u64 v[96:97], v[40:41], 0, s[26:27]
	global_load_lds_dwordx4 v[96:97], off
	v_mfma_f32_16x16x32_f16 v[18:21], v[54:57], v[74:77], v[18:21]
	s_add_u32 m0, s30, 0x2000
	v_lshl_add_u64 v[96:97], v[38:39], 0, s[26:27]
	global_load_lds_dwordx4 v[96:97], off
	v_mfma_f32_16x16x32_f16 v[14:17], v[84:87], v[58:61], v[14:17]
	s_mov_b32 m0, s31
	v_lshl_add_u64 v[96:97], v[36:37], 0, s[26:27]
	global_load_lds_dwordx4 v[96:97], off
	v_mfma_f32_16x16x32_f16 v[10:13], v[62:65], v[70:73], v[10:13]
	v_mfma_f32_16x16x32_f16 v[6:9], v[84:87], v[66:69], v[6:9]
	v_mfma_f32_16x16x32_f16 v[2:5], v[62:65], v[74:77], v[2:5]
	s_add_i32 s36, s36, 1
	s_add_u32 s26, s26, 64
	s_add_i32 s28, s37, 1
	s_cmp_lg_u32 s37, 4
	s_cselect_b32 s37, s28, 0
	s_add_i32 s28, s38, 1
	s_cmp_lg_u32 s38, 4
	s_cselect_b32 s38, s28, 0
	s_waitcnt vmcnt(9)
	s_waitcnt lgkmcnt(0)
	s_barrier
	s_lshl_b32 s28, s38, 15
	v_or_b32_e32 v53, s28, v50
	v_add_u32_e32 v88, s28, v92
	v_add_u32_e32 v53, v53, v52
	v_add_u32_e32 v89, s28, v93
	v_cndmask_b32_e64 v88, v88, v95, s[42:43]
	v_add_u32_e32 v95, 64, v95
	ds_read_b128 v[54:57], v53
	ds_read_b128 v[58:61], v88 offset:16384
	v_mfma_f32_16x16x32_f16 v[14:17], v[108:111], v[104:107], v[14:17]
	ds_read_b128 v[62:65], v53 offset:1024
	v_mfma_f32_16x16x32_f16 v[30:33], v[100:103], v[104:107], v[30:33]
	ds_read_b128 v[66:69], v89 offset:16384
	v_mfma_f32_16x16x32_f16 v[22:25], v[100:103], v[112:115], v[22:25]
	ds_read_b128 v[70:73], v88 offset:18432
	v_mfma_f32_16x16x32_f16 v[6:9], v[108:111], v[112:115], v[6:9]
	ds_read_b128 v[74:77], v89 offset:18432
	v_mfma_f32_16x16x32_f16 v[26:29], v[100:103], v[116:119], v[26:29]
	ds_read_b128 v[80:83], v53 offset:8192
	v_mfma_f32_16x16x32_f16 v[30:33], v[124:127], v[104:107], v[30:33]
	ds_read_b128 v[84:87], v53 offset:9216
	v_mfma_f32_16x16x32_f16 v[22:25], v[124:127], v[112:115], v[22:25]
	v_mfma_f32_16x16x32_f16 v[18:21], v[100:103], v[120:123], v[18:21]
	v_mfma_f32_16x16x32_f16 v[14:17], v[128:131], v[104:107], v[14:17]
	v_mfma_f32_16x16x32_f16 v[10:13], v[108:111], v[116:119], v[10:13]
	v_mfma_f32_16x16x32_f16 v[6:9], v[128:131], v[112:115], v[6:9]
	v_mfma_f32_16x16x32_f16 v[2:5], v[108:111], v[120:123], v[2:5]
	s_add_i32 s36, s36, 1
	s_add_u32 s26, s26, 64
	s_add_i32 s28, s37, 1
	s_cmp_lg_u32 s37, 4
	s_cselect_b32 s37, s28, 0
	s_add_i32 s28, s38, 1
	s_cmp_lg_u32 s38, 4
	s_cselect_b32 s38, s28, 0
	s_waitcnt vmcnt(6)
	s_waitcnt lgkmcnt(0)
	s_barrier
	s_lshl_b32 s28, s38, 15
	v_or_b32_e32 v53, s28, v50
	v_add_u32_e32 v88, s28, v92
	v_add_u32_e32 v53, v53, v52
	v_add_u32_e32 v89, s28, v93
	v_cndmask_b32_e64 v88, v88, v95, s[42:43]
	v_add_u32_e32 v95, 64, v95
	ds_read_b128 v[100:103], v53
	ds_read_b128 v[104:107], v88 offset:16384
	v_mfma_f32_16x16x32_f16 v[14:17], v[62:65], v[58:61], v[14:17]
	ds_read_b128 v[108:111], v53 offset:1024
	v_mfma_f32_16x16x32_f16 v[30:33], v[54:57], v[58:61], v[30:33]
	ds_read_b128 v[112:115], v89 offset:16384
	v_mfma_f32_16x16x32_f16 v[22:25], v[54:57], v[66:69], v[22:25]
	ds_read_b128 v[116:119], v88 offset:18432
	v_mfma_f32_16x16x32_f16 v[6:9], v[62:65], v[66:69], v[6:9]
	ds_read_b128 v[120:123], v89 offset:18432
	v_mfma_f32_16x16x32_f16 v[26:29], v[54:57], v[70:73], v[26:29]
	ds_read_b128 v[124:127], v53 offset:8192
	v_mfma_f32_16x16x32_f16 v[30:33], v[80:83], v[58:61], v[30:33]
	ds_read_b128 v[128:131], v53 offset:9216
	v_mfma_f32_16x16x32_f16 v[22:25], v[80:83], v[66:69], v[22:25]
	v_mfma_f32_16x16x32_f16 v[18:21], v[54:57], v[74:77], v[18:21]
	v_mfma_f32_16x16x32_f16 v[14:17], v[84:87], v[58:61], v[14:17]
	v_mfma_f32_16x16x32_f16 v[10:13], v[62:65], v[70:73], v[10:13]
	v_mfma_f32_16x16x32_f16 v[6:9], v[84:87], v[66:69], v[6:9]
	v_mfma_f32_16x16x32_f16 v[2:5], v[62:65], v[74:77], v[2:5]
	s_add_i32 s36, s36, 1
	s_add_u32 s26, s26, 64
	s_add_i32 s28, s37, 1
	s_cmp_lg_u32 s37, 4
	s_cselect_b32 s37, s28, 0
	s_add_i32 s28, s38, 1
	s_cmp_lg_u32 s38, 4
	s_cselect_b32 s38, s28, 0
	s_waitcnt vmcnt(3)
	s_waitcnt lgkmcnt(0)
	s_barrier
	s_lshl_b32 s28, s38, 15
	v_or_b32_e32 v53, s28, v50
	v_add_u32_e32 v88, s28, v92
	v_add_u32_e32 v53, v53, v52
	v_add_u32_e32 v89, s28, v93
	v_cndmask_b32_e64 v88, v88, v95, s[42:43]
	v_add_u32_e32 v95, 64, v95
	ds_read_b128 v[54:57], v53
	ds_read_b128 v[58:61], v88 offset:16384
	v_mfma_f32_16x16x32_f16 v[14:17], v[108:111], v[104:107], v[14:17]
	ds_read_b128 v[62:65], v53 offset:1024
	v_mfma_f32_16x16x32_f16 v[30:33], v[100:103], v[104:107], v[30:33]
	ds_read_b128 v[66:69], v89 offset:16384
	v_mfma_f32_16x16x32_f16 v[22:25], v[100:103], v[112:115], v[22:25]
	ds_read_b128 v[70:73], v88 offset:18432
	v_mfma_f32_16x16x32_f16 v[6:9], v[108:111], v[112:115], v[6:9]
	ds_read_b128 v[74:77], v89 offset:18432
	v_mfma_f32_16x16x32_f16 v[26:29], v[100:103], v[116:119], v[26:29]
	ds_read_b128 v[80:83], v53 offset:8192
	v_mfma_f32_16x16x32_f16 v[30:33], v[124:127], v[104:107], v[30:33]
	ds_read_b128 v[84:87], v53 offset:9216
	v_mfma_f32_16x16x32_f16 v[22:25], v[124:127], v[112:115], v[22:25]
	v_mfma_f32_16x16x32_f16 v[18:21], v[100:103], v[120:123], v[18:21]
	v_mfma_f32_16x16x32_f16 v[14:17], v[128:131], v[104:107], v[14:17]
	v_mfma_f32_16x16x32_f16 v[10:13], v[108:111], v[116:119], v[10:13]
	v_mfma_f32_16x16x32_f16 v[6:9], v[128:131], v[112:115], v[6:9]
	v_mfma_f32_16x16x32_f16 v[2:5], v[108:111], v[120:123], v[2:5]
	s_add_i32 s36, s36, 1
	s_add_u32 s26, s26, 64
	s_add_i32 s28, s37, 1
	s_cmp_lg_u32 s37, 4
	s_cselect_b32 s37, s28, 0
	s_add_i32 s28, s38, 1
	s_cmp_lg_u32 s38, 4
	s_cselect_b32 s38, s28, 0
	s_waitcnt vmcnt(0)
	s_waitcnt lgkmcnt(0)
	s_barrier
	s_lshl_b32 s28, s38, 15
	v_or_b32_e32 v53, s28, v50
	v_add_u32_e32 v88, s28, v92
	v_add_u32_e32 v53, v53, v52
	v_add_u32_e32 v89, s28, v93
	v_cndmask_b32_e64 v88, v88, v95, s[42:43]
	v_add_u32_e32 v95, 64, v95
	ds_read_b128 v[100:103], v53
	ds_read_b128 v[104:107], v88 offset:16384
	v_mfma_f32_16x16x32_f16 v[14:17], v[62:65], v[58:61], v[14:17]
	ds_read_b128 v[108:111], v53 offset:1024
	v_mfma_f32_16x16x32_f16 v[30:33], v[54:57], v[58:61], v[30:33]
	ds_read_b128 v[112:115], v89 offset:16384
	v_mfma_f32_16x16x32_f16 v[22:25], v[54:57], v[66:69], v[22:25]
	ds_read_b128 v[116:119], v88 offset:18432
	v_mfma_f32_16x16x32_f16 v[6:9], v[62:65], v[66:69], v[6:9]
	ds_read_b128 v[120:123], v89 offset:18432
	v_mfma_f32_16x16x32_f16 v[26:29], v[54:57], v[70:73], v[26:29]
	ds_read_b128 v[124:127], v53 offset:8192
	v_mfma_f32_16x16x32_f16 v[30:33], v[80:83], v[58:61], v[30:33]
	ds_read_b128 v[128:131], v53 offset:9216
	v_mfma_f32_16x16x32_f16 v[22:25], v[80:83], v[66:69], v[22:25]
	v_mfma_f32_16x16x32_f16 v[18:21], v[54:57], v[74:77], v[18:21]
	v_mfma_f32_16x16x32_f16 v[14:17], v[84:87], v[58:61], v[14:17]
	v_mfma_f32_16x16x32_f16 v[10:13], v[62:65], v[70:73], v[10:13]
	v_mfma_f32_16x16x32_f16 v[6:9], v[84:87], v[66:69], v[6:9]
	v_mfma_f32_16x16x32_f16 v[2:5], v[62:65], v[74:77], v[2:5]
	s_add_i32 s36, s36, 1
	s_add_u32 s26, s26, 64
	s_add_i32 s28, s37, 1
	s_cmp_lg_u32 s37, 4
	s_cselect_b32 s37, s28, 0
	s_add_i32 s28, s38, 1
	s_cmp_lg_u32 s38, 4
	s_cselect_b32 s38, s28, 0
	s_waitcnt lgkmcnt(0)
	v_mfma_f32_16x16x32_f16 v[14:17], v[108:111], v[104:107], v[14:17]
	v_mfma_f32_16x16x32_f16 v[30:33], v[100:103], v[104:107], v[30:33]
	v_mfma_f32_16x16x32_f16 v[22:25], v[100:103], v[112:115], v[22:25]
	v_mfma_f32_16x16x32_f16 v[6:9], v[108:111], v[112:115], v[6:9]
	v_mfma_f32_16x16x32_f16 v[26:29], v[100:103], v[116:119], v[26:29]
	v_mfma_f32_16x16x32_f16 v[30:33], v[124:127], v[104:107], v[30:33]
	v_mfma_f32_16x16x32_f16 v[22:25], v[124:127], v[112:115], v[22:25]
	v_mfma_f32_16x16x32_f16 v[18:21], v[100:103], v[120:123], v[18:21]
	v_mfma_f32_16x16x32_f16 v[14:17], v[128:131], v[104:107], v[14:17]
	v_mfma_f32_16x16x32_f16 v[10:13], v[108:111], v[116:119], v[10:13]
	v_mfma_f32_16x16x32_f16 v[6:9], v[128:131], v[112:115], v[6:9]
	v_mfma_f32_16x16x32_f16 v[2:5], v[108:111], v[120:123], v[2:5]
	s_nop 1
